# v50 + G5: with a successor unit, the last two row blocks of the epilogue are finished in the next unit's peeled K-iteration 0 (seg-2 load phase) instead of the epilogue; ROWRS prefetch moved after ite
# baseline (speedup 1.0000x reference)
; #define PG8_STAGE_A(b, h, ptr, NX) do { if constexpr (Sched::GATHER) { unsigned gs_[2]; gs_[0] = ((NX) && last_) ? gN[h][0] : gA[h][0]; gs_[1] = ((NX) && last_) ? gN[h][1] : gA[h][1]; PG8_STAGE(PG8_SA(b, h), ptr, gs_); } \
;         else PG8_STAGE(PG8_SA(b, h), (ptr) + ((h) ? hstep : (size_t)0), voffA); } while (0)
; #define PG8_STAGE(bufoff, gbase, voff) do { _Pragma("unroll") for (int _i = 0; _i < 2; ++_i) \
;         __builtin_amdgcn_global_load_lds((const unsigned*)((const char*)(gbase) + (voff)[_i]), (PG8_LAS unsigned*)(lds + (bufoff) + ldsw + _i * 8192), 16, 0, 0); } while (0)
; #define PG8_WAIT_V(n) asm volatile("s_waitcnt vmcnt(" #n ")" ::: "memory")
; #define PG8_BAR __builtin_amdgcn_s_barrier()
; template <class Epi, class Sched, bool ALIGN_EPI = false, bool SP2 = false>
; __device__ __forceinline__ void gemm_phase(PG8_LAS unsigned char* lds, const Gemm g, const Sched& S, const Epi& E, const bool skip_epi = false) {
;     ...
;     const unsigned ldsw = (unsigned)wid * 1024u;
;     const int aoff = lds_byte(wr * 64 + fr, fq * 8), boff = lds_byte(wc * 32 + fr, fq * 8);
;     ...
;     if constexpr (SP2) {
;         PG8_STAGE(PG8_SB(0, 0), cB, voffB); PG8_STAGE(PG8_SB(0, 1), cB + hstep, voffB); PG8_STAGE_A(0, 0, cA, false); PG8_STAGE_A(0, 1, cA, false);
;         if (wr == 1) PG8_BAR;
;         PG8_WAIT_V(2); PG8_BAR;
;         PG8_STAGE(PG8_SB(1, 0), cB + kstep, voffB); PG8_STAGE_A(1, 0, cA + kstep, false); PG8_STAGE(PG8_SB(1, 1), cB + hstep + kstep, voffB);
;         PG8_WAIT_V(6); PG8_BAR;
;     } else {
;         PG8_STAGE(PG8_SB(0, 0), cB, voffB); PG8_STAGE_A(0, 0, cA, false); PG8_STAGE(PG8_SB(0, 1), cB + hstep, voffB); PG8_STAGE_A(0, 1, cA, false);
;         if (wr == 1) PG8_BAR;
;         PG8_WAIT_V(4); PG8_BAR;
;         PG8_STAGE(PG8_SB(1, 0), cB + kstep, voffB); PG8_STAGE_A(1, 0, cA + kstep, false); PG8_STAGE(PG8_SB(1, 1), cB + hstep + kstep, voffB);
;         PG8_WAIT_V(6); PG8_BAR;
.LBB0_1716:
	s_lshl_b32 s6, s6, 5
	s_mov_b64 s[22:23], 0x80
	s_and_b32 s28, s6, 0x60
	s_add_i32 m0, s37, 0x18000
	v_lshl_add_u64 v[4:5], v[4:5], 0, s[22:23]
	s_lshl_b32 s54, s7, 6
	s_lshl_b32 s27, s7, 13
	s_lshl_b32 s29, s28, 7
	s_waitcnt vmcnt(2)
	s_barrier
	global_load_lds_dwordx4 v[4:5], off
	s_add_i32 m0, s37, 0x1a000
	s_add_u32 s24, s78, 0x1aa00080
	v_lshl_add_u64 v[2:3], v[2:3], 0, s[22:23]
	s_addc_u32 s25, s79, 0
	s_add_i32 s55, s37, 0x8000
	s_add_i32 s56, s37, 0xa000
	global_load_lds_dwordx4 v[2:3], off
	v_lshl_add_u64 v[2:3], s[24:25], 0, v[132:133]
	s_mov_b32 m0, s55
	s_add_u32 s6, s40, 0x40080
	global_load_lds_dwordx4 v[2:3], off
	v_lshl_add_u64 v[2:3], s[24:25], 0, v[144:145]
	s_mov_b32 m0, s56
	s_addc_u32 s7, s41, 0
	global_load_lds_dwordx4 v[2:3], off
	s_add_i32 m0, s37, 0x1c000
	v_lshl_add_u64 v[2:3], s[6:7], 0, v[134:135]
	global_load_lds_dwordx4 v[2:3], off
	v_lshl_add_u64 v[2:3], s[6:7], 0, v[136:137]
	s_add_i32 m0, s37, 0x1e000
	v_and_b32_e32 v145, 15, v6
	global_load_lds_dwordx4 v[2:3], off
	v_and_b32_e32 v2, 48, v6
	v_lshlrev_b32_e32 v3, 2, v6
	v_lshl_or_b32 v2, v145, 6, v2
	v_and_b32_e32 v3, 32, v3
	s_waitcnt vmcnt(6)
	s_cmpk_lt_u32 s26, 0x100
	v_bitop3_b32 v4, v2, s27, v3 bitop3:0xde
	v_bitop3_b32 v154, s29, v2, v3 bitop3:0xf6
	s_cselect_b64 s[26:27], -1, 0
	v_and_b32_e32 v2, 3, v6
	v_and_b32_e32 v3, 60, v6
	s_add_i32 s58, 0, 0x10000
	s_add_i32 s59, 0, 0x14000
	v_bfe_u32 v155, v6, 2, 4
	v_lshl_or_b32 v156, v2, 6, v3
	s_ashr_i32 s57, s97, 31
	v_lshl_or_b32 v157, v2, 3, s28
	v_mov_b64_e32 v[138:139], s[4:5]
	v_add_u32_e32 v158, s58, v154
	v_add_u32_e32 v159, s59, v154
	v_add_u32_e32 v160, 0, v4
	s_movk_i32 s60, 0x1c00
	v_mov_b32_e32 v161, v133
	v_mov_b32_e32 v162, v133
	v_mov_b32_e32 v163, v133
	v_mov_b32_e32 v164, v133
	v_mov_b32_e32 v130, v132
	s_barrier
	s_mov_b32 s98, 0
	s_branch .LBB0_1719

; #define PG8_GIDX(G_, PM_) do { if constexpr (Sched::GATHER) { _Pragma("unroll") for (int h_ = 0; h_ < 2; ++h_) _Pragma("unroll") for (int i_ = 0; i_ < 2; ++i_) { int R_, C_; stage_rc(tid * 16 + i_ * 8192, R_, C_); \
;         const int src_ = S.rowsrc[(PM_) * BM + h_ * HALF + R_]; G_[h_][i_] = (unsigned)(src_ * K + C_) * 2u; } } } while (0)
; #define PG8_LDA(dst, b, h) do { _Pragma("unroll") for (int m = 0; m < 4; ++m) _Pragma("unroll") for (int k = 0; k < 2; ++k) dst[m][k] = *(const PG8_LAS bf16x8*)(lds + PG8_SA(b, h) + aoff + m * 2048 + k * 1024); } while (0)
;     __device__ bool next(int i, Unit& u) const {
;         const int nwg = npan * NT; const long L = (long)i * G + c; if (L >= nwg) return false;
;         int wgid = (int)L; { const int q = nwg / NXCD, r = nwg % NXCD, xcd = wgid % NXCD, off = wgid / NXCD; wgid = (xcd < r ? xcd * (q + 1) : r * (q + 1) + (xcd - r) * q) + off; }
;         const int nig = GP * NT, grp = wgid / nig, fm = grp * GP, gsz = (npan - fm) < GP ? (npan - fm) : GP; const int rr = wgid % nig;
;         const int p = fm + rr % gsz; u.pm = p; u.pn = panel_e[p] * NT + rr / gsz; u.ko = 0; return true;
; template <class Epi, class Sched, bool ALIGN_EPI = false, bool SP2 = false>
; __device__ __forceinline__ void gemm_phase(PG8_LAS unsigned char* lds, const Gemm g, const Sched& S, const Epi& E, const bool skip_epi = false) {
;     ...
;         const bool has_next = S.next(ui + 1, nxt);
;         if (has_next) PG8_GIDX(gN, nxt.pm);
;         const char* nA = has_next ? (const char*)g.A + (size_t)nxt.pm * pmstepA + nxt.ko : cA; const char* nB = has_next ? (const char*)g.Bt + (size_t)nxt.pn * tstep + nxt.ko : cB;
;         for (int t = 0; t < nt; t += 2) {
;             const bool last = (t == nt - 2); last_ = last && has_next;
;             const char* a1 = cA + (size_t)(t + 1) * kstep;
;             const char* a2 = last ? nA : cA + (size_t)(t + 2) * kstep; const char* b2 = last ? nB : cB + (size_t)(t + 2) * kstep;
;             const char* a3 = a2 + kstep; const char* b3 = b2 + kstep;
;             if (last && has_next) S.a_ready(nxt);
;             if constexpr (SP2) {
;             PG8_LDB(B0, 0, 0); PG8_LDB(B1, 0, 1); PG8_SCHED; PG8_LDA(At, 0, 0); PG8_STAGE_A(1, 1, a1, false);
;             PG8_WAIT_V(8); PG8_WAIT_L(0); PG8_BAR; PG8_MMA(0, 0, At, B0); PG8_MMA(0, 1, At, B1); PG8_BAR; PG8_SCHED;
.LBB0_1724:
	s_ashr_i32 s4, s28, 3
	s_add_i32 s4, s30, s4
	s_mul_hi_i32 s5, s4, 0x92492493
	s_add_i32 s5, s5, s4
	s_lshr_b32 s28, s5, 31
	s_ashr_i32 s5, s5, 6
	s_add_i32 s5, s5, s28
	s_lshl_b32 s28, s5, 2
	s_sub_i32 s29, s2, s28
	s_min_i32 s29, s29, 4
	s_abs_i32 s30, s29
	v_cvt_f32_u32_e32 v66, s30
	s_sub_i32 s34, 0, s30
	s_mulk_i32 s5, 0x70
	s_sub_i32 s4, s4, s5
	v_rcp_iflag_f32_e32 v66, v66
	s_abs_i32 s5, s4
	s_xor_b32 s31, s4, s29
	s_ashr_i32 s31, s31, 31
	v_mul_f32_e32 v66, 0x4f7ffffe, v66
	v_cvt_u32_f32_e32 v66, v66
	s_nop 0
	v_readfirstlane_b32 s35, v66
	s_mul_i32 s34, s34, s35
	s_mul_hi_u32 s34, s35, s34
	s_add_i32 s35, s35, s34
	s_mul_hi_u32 s34, s5, s35
	s_mul_i32 s35, s34, s30
	s_sub_i32 s5, s5, s35
	s_add_i32 s42, s34, 1
	s_sub_i32 s35, s5, s30
	s_cmp_ge_u32 s5, s30
	s_cselect_b32 s34, s42, s34
	s_cselect_b32 s5, s35, s5
	s_add_i32 s35, s34, 1
	s_cmp_ge_u32 s5, s30
	s_cselect_b32 s5, s35, s34
	s_xor_b32 s5, s5, s31
	s_sub_i32 s30, s5, s31
	s_mul_i32 s5, s30, s29
	s_sub_i32 s4, s4, s5
	s_add_i32 s28, s28, s4
	s_ashr_i32 s29, s28, 31
	s_lshl_b64 s[4:5], s[28:29], 2
	s_add_u32 s4, s14, s4
	s_addc_u32 s5, s15, s5
	global_load_dword v250, v133, s[4:5]
.LBB0_1725:
	s_nop 0
	v_cndmask_b32_e64 v66, 0, 1, s[6:7]
	v_cmp_ne_u32_e64 s[4:5], 1, v66
	s_andn2_b64 vcc, exec, s[6:7]
	s_cbranch_vccnz .Lg5_zero
	s_lshl_b32 s29, s28, 8
	v_add_u32_e32 v66, s29, v1
	v_add_u32_e32 v68, s29, v151
	s_bitset1_b32 s29, 7
	v_ashrrev_i32_e32 v67, 31, v66
	v_ashrrev_i32_e32 v69, 31, v68
	v_add_u32_e32 v70, s29, v1
	v_add_u32_e32 v72, s29, v151
	v_lshl_add_u64 v[66:67], v[66:67], 2, s[20:21]
	v_lshl_add_u64 v[68:69], v[68:69], 2, s[20:21]
	v_ashrrev_i32_e32 v71, 31, v70
	v_ashrrev_i32_e32 v73, 31, v72
	v_lshl_add_u64 v[70:71], v[70:71], 2, s[20:21]
	v_lshl_add_u64 v[72:73], v[72:73], 2, s[20:21]
	global_load_dword v229, v[66:67], off
	s_nop 0
	global_load_dword v251, v[68:69], off
	s_nop 0
	global_load_dword v252, v[70:71], off
	global_load_dword v253, v[72:73], off
.Lg5_zero:
.LBB0_1727:
	s_mov_b32 s29, s41
	s_mov_b32 s31, s40
	v_mov_b32_e32 v143, v133
	v_mov_b32_e32 v141, v133
	s_add_u32 s61, s40, 0x100
	v_lshl_add_u64 v[146:147], s[24:25], 0, v[140:141]
	v_lshl_add_u64 v[148:149], s[24:25], 0, v[142:143]
	s_addc_u32 s62, s41, 0
	s_mov_b32 s63, -2
	s_mov_b64 s[40:41], 0
	ds_read_b128 v[166:169], v158
	ds_read_b128 v[170:173], v158 offset:1024
	ds_read_b128 v[174:177], v158 offset:2048
	ds_read_b128 v[178:181], v158 offset:3072
	ds_read_b128 v[182:185], v159
	ds_read_b128 v[186:189], v159 offset:1024
	ds_read_b128 v[190:193], v159 offset:2048
	ds_read_b128 v[194:197], v159 offset:3072
	s_add_u32 s42, s78, s40
	s_addc_u32 s43, s79, s41
	s_add_u32 s44, s42, 0x1aa00100
	s_addc_u32 s45, s43, 0
	s_add_u32 s66, s61, s40
	s_addc_u32 s67, s62, s41
	s_cmpk_eq_i32 s40, 0x700
	s_cselect_b64 s[64:65], -1, 0
	s_and_b64 s[42:43], s[64:65], exec
	s_cselect_b32 s45, s87, s45
	s_cselect_b32 s44, s86, s44
	s_cselect_b32 s42, s31, s66
	s_cselect_b32 s43, s29, s67
	s_and_b64 vcc, s[6:7], s[64:65]
	v_lshl_add_u64 v[226:227], v[148:149], 0, s[40:41]
	s_add_i32 m0, s37, 0xc000
	ds_read_b128 v[198:201], v160
	ds_read_b128 v[202:205], v160 offset:1024
	ds_read_b128 v[206:209], v160 offset:2048
	ds_read_b128 v[210:213], v160 offset:3072
	ds_read_b128 v[214:217], v160 offset:4096
	ds_read_b128 v[218:221], v160 offset:5120
	ds_read_b128 v[222:225], v160 offset:6144
	ds_read_b128 v[230:233], v160 offset:7168
	global_load_lds_dwordx4 v[226:227], off
	v_lshl_add_u64 v[226:227], v[146:147], 0, s[40:41]
	s_add_i32 m0, s37, 0xe000
	s_nop 0
	global_load_lds_dwordx4 v[226:227], off
	s_waitcnt vmcnt(8)
	s_waitcnt lgkmcnt(0)
	s_barrier
	s_setprio 1
	s_waitcnt lgkmcnt(0)
	v_mfma_f32_16x16x32_bf16 v[126:129], v[166:169], v[198:201], 0
	v_mfma_f32_16x16x32_bf16 v[122:125], v[174:177], v[198:201], 0
	v_mfma_f32_16x16x32_bf16 v[110:113], v[166:169], v[206:209], 0
	v_mfma_f32_16x16x32_bf16 v[106:109], v[174:177], v[206:209], 0
	v_mfma_f32_16x16x32_bf16 v[94:97], v[166:169], v[214:217], 0
	v_mfma_f32_16x16x32_bf16 v[90:93], v[174:177], v[214:217], 0
	v_mfma_f32_16x16x32_bf16 v[78:81], v[166:169], v[222:225], 0
	v_mfma_f32_16x16x32_bf16 v[74:77], v[174:177], v[222:225], 0
	v_mfma_f32_16x16x32_bf16 v[126:129], v[170:173], v[202:205], v[126:129]
	v_mfma_f32_16x16x32_bf16 v[122:125], v[178:181], v[202:205], v[122:125]
	v_mfma_f32_16x16x32_bf16 v[110:113], v[170:173], v[210:213], v[110:113]
	v_mfma_f32_16x16x32_bf16 v[106:109], v[178:181], v[210:213], v[106:109]
	v_mfma_f32_16x16x32_bf16 v[94:97], v[170:173], v[218:221], v[94:97]
	v_mfma_f32_16x16x32_bf16 v[90:93], v[178:181], v[218:221], v[90:93]
	v_mfma_f32_16x16x32_bf16 v[78:81], v[170:173], v[230:233], v[78:81]
	v_mfma_f32_16x16x32_bf16 v[74:77], v[178:181], v[230:233], v[74:77]
	s_setprio 0
	s_setprio 1
	v_mfma_f32_16x16x32_bf16 v[118:121], v[182:185], v[198:201], 0
	v_mfma_f32_16x16x32_bf16 v[114:117], v[190:193], v[198:201], 0
	v_mfma_f32_16x16x32_bf16 v[102:105], v[182:185], v[206:209], 0
	v_mfma_f32_16x16x32_bf16 v[98:101], v[190:193], v[206:209], 0
	v_mfma_f32_16x16x32_bf16 v[86:89], v[182:185], v[214:217], 0
	v_mfma_f32_16x16x32_bf16 v[82:85], v[190:193], v[214:217], 0
	v_mfma_f32_16x16x32_bf16 v[70:73], v[182:185], v[222:225], 0
	v_mfma_f32_16x16x32_bf16 v[66:69], v[190:193], v[222:225], 0
	v_mfma_f32_16x16x32_bf16 v[118:121], v[186:189], v[202:205], v[118:121]
	v_mfma_f32_16x16x32_bf16 v[114:117], v[194:197], v[202:205], v[114:117]
	v_mfma_f32_16x16x32_bf16 v[102:105], v[186:189], v[210:213], v[102:105]
	v_mfma_f32_16x16x32_bf16 v[98:101], v[194:197], v[210:213], v[98:101]
	v_mfma_f32_16x16x32_bf16 v[86:89], v[186:189], v[218:221], v[86:89]
	v_mfma_f32_16x16x32_bf16 v[82:85], v[194:197], v[218:221], v[82:85]
	v_mfma_f32_16x16x32_bf16 v[70:73], v[186:189], v[230:233], v[70:73]
	v_mfma_f32_16x16x32_bf16 v[66:69], v[194:197], v[230:233], v[66:69]
	s_setprio 0
	s_barrier
; __device__ __forceinline__ unsigned cvt_pk_bf16(float lo, float hi) { const f32x2c_t v = {lo, hi}; return __builtin_bit_cast(unsigned, __builtin_convertvector(v, bf16x2c_t)); }
; __device__ __forceinline__ float silu_f(float a) { return a * __builtin_amdgcn_rcpf(1.0f + __builtin_amdgcn_exp2f(a * -1.4426950408889634f)); }
; #define PG8_STAGE_A(b, h, ptr, NX) do { if constexpr (Sched::GATHER) { unsigned gs_[2]; gs_[0] = ((NX) && last_) ? gN[h][0] : gA[h][0]; gs_[1] = ((NX) && last_) ? gN[h][1] : gA[h][1]; PG8_STAGE(PG8_SA(b, h), ptr, gs_); } \
;         else PG8_STAGE(PG8_SA(b, h), (ptr) + ((h) ? hstep : (size_t)0), voffA); } while (0)
; #define PG8_STAGE(bufoff, gbase, voff) do { _Pragma("unroll") for (int _i = 0; _i < 2; ++_i) \
;         __builtin_amdgcn_global_load_lds((const unsigned*)((const char*)(gbase) + (voff)[_i]), (PG8_LAS unsigned*)(lds + (bufoff) + ldsw + _i * 8192), 16, 0, 0); } while (0)
; #define PG8_BAR __builtin_amdgcn_s_barrier()
;     __device__ __forceinline__ void operator()(const f32x4 (&acc)[2][2][4][2], const Unit& u, int wr, int wc, int fr, int fq) const {
;     ...
;             for (int m = 0; m < 4; ++m) { const int row = row0 + ai * HALF + m * 16; const float rs = rs8[ai][m];
;                 const f32x4 a0 = acc[ai][0][m][0] * rs, a1 = acc[ai][0][m][1] * rs, b0 = acc[ai][1][m][0] * rs, b1 = acc[ai][1][m][1] * rs;
;                 f32x4 g0, g1;
; #pragma unroll
;                 for (int j = 0; j < 4; ++j) { g0[j] = silu_f(a0[j]) * b0[j]; g1[j] = silu_f(a1[j]) * b1[j]; }
;                 u32x4 w; w.x = cvt_pk_bf16(g0[0], g0[1]); w.y = cvt_pk_bf16(g0[2], g0[3]); w.z = cvt_pk_bf16(g1[0], g1[1]); w.w = cvt_pk_bf16(g1[2], g1[3]);
;                 w = lane_perm(w, qs4); u32x4* dst = (u32x4*)(O + (size_t)(rowS + ai * HALF + m * 16) * ldo + colS); (void)row;
;                 if constexpr (MOE) __builtin_nontemporal_store(w, dst); else *dst = w; } }
; template <class Epi, class Sched, bool ALIGN_EPI = false, bool SP2 = false>
; __device__ __forceinline__ void gemm_phase(PG8_LAS unsigned char* lds, const Gemm g, const Sched& S, const Epi& E, const bool skip_epi = false) {
;     ...
;             PG8_LDA(At, 0, 1); PG8_STAGE(PG8_SB(0, 0), b2, voffB); PG8_STAGE(PG8_SB(0, 1), b2 + hstep, voffB); PG8_STAGE_A(0, 0, a2, true);
;             PG8_WAIT_V(8); PG8_WAIT_L(0); PG8_BAR; PG8_MMA(1, 0, At, B0); PG8_MMA(1, 1, At, B1); PG8_BAR; PG8_SCHED;
	s_add_i32 s64, s58, s50
	v_lshl_add_u64 v[226:227], s[42:43], 0, v[134:135]
	s_mov_b32 m0, s64
	ds_read_b128 v[198:201], v160 offset:16384
	ds_read_b128 v[202:205], v160 offset:17408
	ds_read_b128 v[206:209], v160 offset:18432
	ds_read_b128 v[210:213], v160 offset:19456
	ds_read_b128 v[214:217], v160 offset:20480
	ds_read_b128 v[218:221], v160 offset:21504
	ds_read_b128 v[222:225], v160 offset:22528
	ds_read_b128 v[230:233], v160 offset:23552
	s_cmp_eq_u32 s98, 0
	s_cbranch_scc1 .Lg5_nodefer
	v_exp_f32_e32 v22, v22
	v_exp_f32_e32 v23, v23
	v_exp_f32_e32 v24, v24
	v_exp_f32_e32 v25, v25
	v_exp_f32_e32 v18, v18
	v_exp_f32_e32 v19, v19
	v_exp_f32_e32 v20, v20
	v_exp_f32_e32 v21, v21
	v_exp_f32_e32 v6, v6
	v_exp_f32_e32 v7, v7
	v_exp_f32_e32 v8, v8
	v_exp_f32_e32 v9, v9
	v_exp_f32_e32 v2, v2
	v_exp_f32_e32 v3, v3
	v_exp_f32_e32 v4, v4
	v_exp_f32_e32 v5, v5
	v_add_f32_e32 v22, 1.0, v22
	v_add_f32_e32 v23, 1.0, v23
	v_add_f32_e32 v24, 1.0, v24
	v_add_f32_e32 v25, 1.0, v25
	v_add_f32_e32 v18, 1.0, v18
	v_add_f32_e32 v19, 1.0, v19
	v_add_f32_e32 v20, 1.0, v20
	v_add_f32_e32 v21, 1.0, v21
	v_add_f32_e32 v6, 1.0, v6
	v_add_f32_e32 v7, 1.0, v7
	v_add_f32_e32 v8, 1.0, v8
	v_add_f32_e32 v9, 1.0, v9
	v_add_f32_e32 v2, 1.0, v2
	v_add_f32_e32 v3, 1.0, v3
	v_add_f32_e32 v4, 1.0, v4
	v_add_f32_e32 v5, 1.0, v5
	v_rcp_f32_e32 v22, v22
	v_rcp_f32_e32 v23, v23
	v_rcp_f32_e32 v24, v24
	v_rcp_f32_e32 v25, v25
	v_rcp_f32_e32 v18, v18
	v_rcp_f32_e32 v19, v19
	v_rcp_f32_e32 v20, v20
	v_rcp_f32_e32 v21, v21
	v_rcp_f32_e32 v6, v6
	v_rcp_f32_e32 v7, v7
	v_rcp_f32_e32 v8, v8
	v_rcp_f32_e32 v9, v9
	v_rcp_f32_e32 v2, v2
	v_rcp_f32_e32 v3, v3
	v_rcp_f32_e32 v4, v4
	v_rcp_f32_e32 v5, v5
	v_pk_mul_f32 v[30:31], v[30:31], v[22:23]
	v_pk_mul_f32 v[32:33], v[32:33], v[24:25]
	v_pk_mul_f32 v[26:27], v[26:27], v[18:19]
	v_pk_mul_f32 v[28:29], v[28:29], v[20:21]
	v_pk_mul_f32 v[14:15], v[14:15], v[6:7]
	v_pk_mul_f32 v[16:17], v[16:17], v[8:9]
	v_pk_mul_f32 v[10:11], v[10:11], v[2:3]
	v_pk_mul_f32 v[12:13], v[12:13], v[4:5]
	v_cvt_pk_bf16_f32 v22, v30, v31
	v_cvt_pk_bf16_f32 v23, v32, v33
	v_cvt_pk_bf16_f32 v24, v26, v27
	v_cvt_pk_bf16_f32 v25, v28, v29
	v_cvt_pk_bf16_f32 v6, v14, v15
	v_cvt_pk_bf16_f32 v7, v16, v17
	v_cvt_pk_bf16_f32 v8, v10, v11
	v_cvt_pk_bf16_f32 v9, v12, v13
	ds_bpermute_b32 v18, v156, v22
	ds_bpermute_b32 v19, v156, v23
	ds_bpermute_b32 v20, v156, v24
	ds_bpermute_b32 v21, v156, v25
	ds_bpermute_b32 v2, v156, v6
	ds_bpermute_b32 v3, v156, v7
	ds_bpermute_b32 v4, v156, v8
	ds_bpermute_b32 v5, v156, v9
	s_waitcnt lgkmcnt(0)
	global_store_dwordx4 v[240:241], v[18:21], off nt
	global_store_dwordx4 v[242:243], v[2:5], off nt
	s_mov_b32 s98, 0
.Lg5_nodefer:
	global_load_lds_dwordx4 v[226:227], off
	s_add_i32 m0, s64, 0x2000
	s_add_u32 s64, s42, 0x40000
	v_lshl_add_u64 v[234:235], s[42:43], 0, v[136:137]
	s_addc_u32 s65, s43, 0
	s_add_i32 s66, s59, s50
	global_load_lds_dwordx4 v[234:235], off
	v_lshl_add_u64 v[236:237], s[64:65], 0, v[134:135]
	s_mov_b32 m0, s66
	v_cndmask_b32_e32 v132, v130, v164, vcc
	global_load_lds_dwordx4 v[236:237], off
	v_lshl_add_u64 v[236:237], s[64:65], 0, v[136:137]
	s_add_i32 m0, s66, 0x2000
	v_lshl_add_u64 v[238:239], s[44:45], 0, v[132:133]
	global_load_lds_dwordx4 v[236:237], off
	s_mov_b32 m0, s37
	v_cndmask_b32_e32 v236, v144, v163, vcc
	global_load_lds_dwordx4 v132, s[44:45]
	s_mov_b32 m0, s39
	v_mov_b32_e32 v237, v133
	global_load_lds_dwordx4 v236, s[44:45]
	s_waitcnt vmcnt(8)
	s_waitcnt lgkmcnt(0)
	v_lshl_add_u64 v[236:237], s[44:45], 0, v[236:237]
	s_barrier
	s_setprio 1
	s_waitcnt lgkmcnt(0)
	v_mfma_f32_16x16x32_bf16 v[62:65], v[166:169], v[198:201], 0
	v_mfma_f32_16x16x32_bf16 v[58:61], v[174:177], v[198:201], 0
	v_mfma_f32_16x16x32_bf16 v[38:41], v[166:169], v[206:209], 0
	v_mfma_f32_16x16x32_bf16 v[34:37], v[174:177], v[206:209], 0
	v_mfma_f32_16x16x32_bf16 v[22:25], v[166:169], v[214:217], 0
	v_mfma_f32_16x16x32_bf16 v[18:21], v[174:177], v[214:217], 0
	v_mfma_f32_16x16x32_bf16 v[6:9], v[166:169], v[222:225], 0
	v_mfma_f32_16x16x32_bf16 v[2:5], v[174:177], v[222:225], 0
	v_mfma_f32_16x16x32_bf16 v[62:65], v[170:173], v[202:205], v[62:65]
	v_mfma_f32_16x16x32_bf16 v[58:61], v[178:181], v[202:205], v[58:61]
	v_mfma_f32_16x16x32_bf16 v[38:41], v[170:173], v[210:213], v[38:41]
	v_mfma_f32_16x16x32_bf16 v[34:37], v[178:181], v[210:213], v[34:37]
	v_mfma_f32_16x16x32_bf16 v[22:25], v[170:173], v[218:221], v[22:25]
	v_mfma_f32_16x16x32_bf16 v[18:21], v[178:181], v[218:221], v[18:21]
	v_mfma_f32_16x16x32_bf16 v[6:9], v[170:173], v[230:233], v[6:9]
	v_mfma_f32_16x16x32_bf16 v[2:5], v[178:181], v[230:233], v[2:5]
	s_setprio 0
	s_setprio 1
	v_mfma_f32_16x16x32_bf16 v[50:53], v[182:185], v[198:201], 0
	v_mfma_f32_16x16x32_bf16 v[42:45], v[190:193], v[198:201], 0
	v_mfma_f32_16x16x32_bf16 v[54:57], v[182:185], v[206:209], 0
	v_mfma_f32_16x16x32_bf16 v[46:49], v[190:193], v[206:209], 0
	v_mfma_f32_16x16x32_bf16 v[30:33], v[182:185], v[214:217], 0
	v_mfma_f32_16x16x32_bf16 v[26:29], v[190:193], v[214:217], 0
	v_mfma_f32_16x16x32_bf16 v[14:17], v[182:185], v[222:225], 0
	v_mfma_f32_16x16x32_bf16 v[10:13], v[190:193], v[222:225], 0
	v_mfma_f32_16x16x32_bf16 v[50:53], v[186:189], v[202:205], v[50:53]
	v_mfma_f32_16x16x32_bf16 v[42:45], v[194:197], v[202:205], v[42:45]
	v_mfma_f32_16x16x32_bf16 v[54:57], v[186:189], v[210:213], v[54:57]
	v_mfma_f32_16x16x32_bf16 v[46:49], v[194:197], v[210:213], v[46:49]
	v_mfma_f32_16x16x32_bf16 v[30:33], v[186:189], v[218:221], v[30:33]
	v_mfma_f32_16x16x32_bf16 v[26:29], v[194:197], v[218:221], v[26:29]
	v_mfma_f32_16x16x32_bf16 v[14:17], v[186:189], v[230:233], v[14:17]
	v_mfma_f32_16x16x32_bf16 v[10:13], v[194:197], v[230:233], v[10:13]
	s_setprio 0
	s_barrier
; #define PG8_STAGE_A(b, h, ptr, NX) do { if constexpr (Sched::GATHER) { unsigned gs_[2]; gs_[0] = ((NX) && last_) ? gN[h][0] : gA[h][0]; gs_[1] = ((NX) && last_) ? gN[h][1] : gA[h][1]; PG8_STAGE(PG8_SA(b, h), ptr, gs_); } \
;         else PG8_STAGE(PG8_SA(b, h), (ptr) + ((h) ? hstep : (size_t)0), voffA); } while (0)
; #define PG8_STAGE(bufoff, gbase, voff) do { _Pragma("unroll") for (int _i = 0; _i < 2; ++_i) \
;         __builtin_amdgcn_global_load_lds((const unsigned*)((const char*)(gbase) + (voff)[_i]), (PG8_LAS unsigned*)(lds + (bufoff) + ldsw + _i * 8192), 16, 0, 0); } while (0)
; #define PG8_LDA(dst, b, h) do { _Pragma("unroll") for (int m = 0; m < 4; ++m) _Pragma("unroll") for (int k = 0; k < 2; ++k) dst[m][k] = *(const PG8_LAS bf16x8*)(lds + PG8_SA(b, h) + aoff + m * 2048 + k * 1024); } while (0)
; #define PG8_LDB(dst, b, h) do { _Pragma("unroll") for (int n = 0; n < 2; ++n) _Pragma("unroll") for (int k = 0; k < 2; ++k) dst[n][k] = *(const PG8_LAS bf16x8*)(lds + PG8_SB(b, h) + boff + n * 2048 + k * 1024); } while (0)
; #define PG8_MMA(ai, bj, At, Bt) do { __builtin_amdgcn_s_setprio(1); _Pragma("unroll") for (int m = 0; m < 4; ++m) _Pragma("unroll") for (int n = 0; n < 2; ++n) _Pragma("unroll") for (int k = 0; k < 2; ++k) \
;         acc[ai][bj][m][n] = __builtin_amdgcn_mfma_f32_16x16x32_bf16(Bt[n][k], At[m][k], acc[ai][bj][m][n], 0, 0, 0); __builtin_amdgcn_s_setprio(0); } while (0)
; #define PG8_WAIT_V(n) asm volatile("s_waitcnt vmcnt(" #n ")" ::: "memory")
; #define PG8_WAIT_L(n) asm volatile("s_waitcnt lgkmcnt(" #n ")" ::: "memory")
; #define PG8_BAR __builtin_amdgcn_s_barrier()
; #define PG8_SCHED __builtin_amdgcn_sched_barrier(0)
; template <class Epi, class Sched, bool ALIGN_EPI = false, bool SP2 = false>
; __device__ __forceinline__ void gemm_phase(PG8_LAS unsigned char* lds, const Gemm g, const Sched& S, const Epi& E, const bool skip_epi = false) {
;     ...
;             PG8_LDB(B0, 1, 0); PG8_LDB(B1, 1, 1); PG8_SCHED; PG8_LDA(At, 1, 0); PG8_STAGE_A(0, 1, a2, true);
;             PG8_WAIT_V(8); PG8_WAIT_L(0); PG8_BAR; PG8_MMA(0, 0, At, B0); PG8_MMA(0, 1, At, B1); PG8_BAR; PG8_SCHED;
;             PG8_LDA(At, 1, 1); PG8_STAGE(PG8_SB(1, 0), b3, voffB); PG8_STAGE(PG8_SB(1, 1), b3 + hstep, voffB); PG8_STAGE_A(1, 0, a3, true);
;             PG8_WAIT_V(8); PG8_WAIT_L(0); PG8_BAR; PG8_MMA(1, 0, At, B0); PG8_MMA(1, 1, At, B1); PG8_BAR; PG8_SCHED;
	s_add_i32 s64, 0, 0x18000
	v_add_u32_e32 v132, s64, v154
	s_add_i32 s65, 0, 0x1c000
	ds_read_b128 v[166:169], v132
	ds_read_b128 v[170:173], v132 offset:1024
	ds_read_b128 v[174:177], v132 offset:2048
	ds_read_b128 v[178:181], v132 offset:3072
	v_add_u32_e32 v132, s65, v154
	ds_read_b128 v[182:185], v132
	ds_read_b128 v[186:189], v132 offset:1024
	ds_read_b128 v[190:193], v132 offset:2048
	ds_read_b128 v[194:197], v132 offset:3072
	s_mov_b32 m0, s51
	v_cndmask_b32_e32 v132, v142, v162, vcc
	ds_read_b128 v[198:201], v160 offset:32768
	ds_read_b128 v[202:205], v160 offset:33792
	ds_read_b128 v[206:209], v160 offset:34816
	ds_read_b128 v[210:213], v160 offset:35840
	ds_read_b128 v[214:217], v160 offset:36864
	ds_read_b128 v[218:221], v160 offset:37888
	ds_read_b128 v[222:225], v160 offset:38912
	ds_read_b128 v[230:233], v160 offset:39936
	v_cndmask_b32_e32 v141, v140, v161, vcc
	global_load_lds_dwordx4 v132, s[44:45]
	s_mov_b32 m0, s52
	s_nop 0
	global_load_lds_dwordx4 v141, s[44:45]
	s_waitcnt vmcnt(8)
	s_waitcnt lgkmcnt(0)
	s_barrier
	s_setprio 1
	s_waitcnt lgkmcnt(0)
	v_mfma_f32_16x16x32_bf16 v[126:129], v[166:169], v[198:201], v[126:129]
	v_mfma_f32_16x16x32_bf16 v[122:125], v[174:177], v[198:201], v[122:125]
	v_mfma_f32_16x16x32_bf16 v[110:113], v[166:169], v[206:209], v[110:113]
	v_mfma_f32_16x16x32_bf16 v[106:109], v[174:177], v[206:209], v[106:109]
	v_mfma_f32_16x16x32_bf16 v[94:97], v[166:169], v[214:217], v[94:97]
	v_mfma_f32_16x16x32_bf16 v[90:93], v[174:177], v[214:217], v[90:93]
	v_mfma_f32_16x16x32_bf16 v[78:81], v[166:169], v[222:225], v[78:81]
	v_mfma_f32_16x16x32_bf16 v[74:77], v[174:177], v[222:225], v[74:77]
	v_mfma_f32_16x16x32_bf16 v[126:129], v[170:173], v[202:205], v[126:129]
	v_mfma_f32_16x16x32_bf16 v[122:125], v[178:181], v[202:205], v[122:125]
	v_mfma_f32_16x16x32_bf16 v[110:113], v[170:173], v[210:213], v[110:113]
	v_mfma_f32_16x16x32_bf16 v[106:109], v[178:181], v[210:213], v[106:109]
	v_mfma_f32_16x16x32_bf16 v[94:97], v[170:173], v[218:221], v[94:97]
	v_mfma_f32_16x16x32_bf16 v[90:93], v[178:181], v[218:221], v[90:93]
	v_mfma_f32_16x16x32_bf16 v[78:81], v[170:173], v[230:233], v[78:81]
	v_mfma_f32_16x16x32_bf16 v[74:77], v[178:181], v[230:233], v[74:77]
	s_setprio 0
	s_setprio 1
	v_mfma_f32_16x16x32_bf16 v[118:121], v[182:185], v[198:201], v[118:121]
	v_mfma_f32_16x16x32_bf16 v[114:117], v[190:193], v[198:201], v[114:117]
	v_mfma_f32_16x16x32_bf16 v[102:105], v[182:185], v[206:209], v[102:105]
	v_mfma_f32_16x16x32_bf16 v[98:101], v[190:193], v[206:209], v[98:101]
	v_mfma_f32_16x16x32_bf16 v[86:89], v[182:185], v[214:217], v[86:89]
	v_mfma_f32_16x16x32_bf16 v[82:85], v[190:193], v[214:217], v[82:85]
	v_mfma_f32_16x16x32_bf16 v[70:73], v[182:185], v[222:225], v[70:73]
	v_mfma_f32_16x16x32_bf16 v[66:69], v[190:193], v[222:225], v[66:69]
	v_mfma_f32_16x16x32_bf16 v[118:121], v[186:189], v[202:205], v[118:121]
	v_mfma_f32_16x16x32_bf16 v[114:117], v[194:197], v[202:205], v[114:117]
	v_mfma_f32_16x16x32_bf16 v[102:105], v[186:189], v[210:213], v[102:105]
	v_mfma_f32_16x16x32_bf16 v[98:101], v[194:197], v[210:213], v[98:101]
	v_mfma_f32_16x16x32_bf16 v[86:89], v[186:189], v[218:221], v[86:89]
	v_mfma_f32_16x16x32_bf16 v[82:85], v[194:197], v[218:221], v[82:85]
	v_mfma_f32_16x16x32_bf16 v[70:73], v[186:189], v[230:233], v[70:73]
	v_mfma_f32_16x16x32_bf16 v[66:69], v[194:197], v[230:233], v[66:69]
	s_setprio 0
	s_barrier
	s_add_i32 s44, s64, s50
	v_lshl_add_u64 v[226:227], v[226:227], 0, s[22:23]
	s_mov_b32 m0, s44
	ds_read_b128 v[198:201], v160 offset:49152
	ds_read_b128 v[202:205], v160 offset:50176
	ds_read_b128 v[206:209], v160 offset:51200
	ds_read_b128 v[210:213], v160 offset:52224
	ds_read_b128 v[214:217], v160 offset:53248
	ds_read_b128 v[218:221], v160 offset:54272
	ds_read_b128 v[222:225], v160 offset:55296
	ds_read_b128 v[230:233], v160 offset:56320
	global_load_lds_dwordx4 v[226:227], off
	s_add_i32 m0, s44, 0x2000
	s_add_u32 s42, s42, 0x40080
	v_lshl_add_u64 v[226:227], v[234:235], 0, s[22:23]
	s_addc_u32 s43, s43, 0
	s_add_i32 s44, s65, s50
	global_load_lds_dwordx4 v[226:227], off
	v_lshl_add_u64 v[226:227], s[42:43], 0, v[134:135]
	s_mov_b32 m0, s44
	s_nop 0
	global_load_lds_dwordx4 v[226:227], off
	v_lshl_add_u64 v[226:227], s[42:43], 0, v[136:137]
	s_add_i32 m0, s44, 0x2000
	s_nop 0
	global_load_lds_dwordx4 v[226:227], off
	v_lshl_add_u64 v[226:227], v[238:239], 0, s[22:23]
	s_mov_b32 m0, s55
	s_nop 0
	global_load_lds_dwordx4 v[226:227], off
	v_lshl_add_u64 v[226:227], v[236:237], 0, s[22:23]
	s_mov_b32 m0, s56
	s_nop 0
	global_load_lds_dwordx4 v[226:227], off
	s_waitcnt vmcnt(8)
	s_waitcnt lgkmcnt(0)
	s_barrier
; #define PG8_STAGE_A(b, h, ptr, NX) do { if constexpr (Sched::GATHER) { unsigned gs_[2]; gs_[0] = ((NX) && last_) ? gN[h][0] : gA[h][0]; gs_[1] = ((NX) && last_) ? gN[h][1] : gA[h][1]; PG8_STAGE(PG8_SA(b, h), ptr, gs_); } \
;         else PG8_STAGE(PG8_SA(b, h), (ptr) + ((h) ? hstep : (size_t)0), voffA); } while (0)
; #define PG8_STAGE(bufoff, gbase, voff) do { _Pragma("unroll") for (int _i = 0; _i < 2; ++_i) \
;         __builtin_amdgcn_global_load_lds((const unsigned*)((const char*)(gbase) + (voff)[_i]), (PG8_LAS unsigned*)(lds + (bufoff) + ldsw + _i * 8192), 16, 0, 0); } while (0)
; #define PG8_LDA(dst, b, h) do { _Pragma("unroll") for (int m = 0; m < 4; ++m) _Pragma("unroll") for (int k = 0; k < 2; ++k) dst[m][k] = *(const PG8_LAS bf16x8*)(lds + PG8_SA(b, h) + aoff + m * 2048 + k * 1024); } while (0)
; #define PG8_MMA(ai, bj, At, Bt) do { __builtin_amdgcn_s_setprio(1); _Pragma("unroll") for (int m = 0; m < 4; ++m) _Pragma("unroll") for (int n = 0; n < 2; ++n) _Pragma("unroll") for (int k = 0; k < 2; ++k) \
;         acc[ai][bj][m][n] = __builtin_amdgcn_mfma_f32_16x16x32_bf16(Bt[n][k], At[m][k], acc[ai][bj][m][n], 0, 0, 0); __builtin_amdgcn_s_setprio(0); } while (0)
; #define PG8_WAIT_V(n) asm volatile("s_waitcnt vmcnt(" #n ")" ::: "memory")
; #define PG8_WAIT_L(n) asm volatile("s_waitcnt lgkmcnt(" #n ")" ::: "memory")
; #define PG8_BAR __builtin_amdgcn_s_barrier()
;     __device__ __forceinline__ void operator()(const f32x4 (&acc)[2][2][4][2], const Unit& u, int wr, int wc, int fr, int fq) const {
;     ...
;                 for (int m = 0; m < 4; ++m) rs8[ai][m] = SS[row0 + ai * HALF + m * 16];
;             asm volatile("" : "+v"(rs8[0][0]), "+v"(rs8[0][1]), "+v"(rs8[0][2]), "+v"(rs8[0][3]), "+v"(rs8[1][0]), "+v"(rs8[1][1]), "+v"(rs8[1][2]), "+v"(rs8[1][3]));
; template <class Epi, class Sched, bool ALIGN_EPI = false, bool SP2 = false>
; __device__ __forceinline__ void gemm_phase(PG8_LAS unsigned char* lds, const Gemm g, const Sched& S, const Epi& E, const bool skip_epi = false) {
;     ...
;             PG8_WAIT_V(8); PG8_WAIT_L(0); PG8_BAR; PG8_MMA(0, 0, At, B0); PG8_MMA(0, 1, At, B1); PG8_BAR; PG8_SCHED;
;             PG8_LDA(At, 1, 1); PG8_STAGE(PG8_SB(1, 0), b3, voffB); PG8_STAGE(PG8_SB(1, 1), b3 + hstep, voffB); PG8_STAGE_A(1, 0, a3, true);
;             PG8_WAIT_V(8); PG8_WAIT_L(0); PG8_BAR; PG8_MMA(1, 0, At, B0); PG8_MMA(1, 1, At, B1); PG8_BAR; PG8_SCHED;
	s_setprio 1
	s_waitcnt lgkmcnt(0)
	v_mfma_f32_16x16x32_bf16 v[62:65], v[166:169], v[198:201], v[62:65]
	v_mfma_f32_16x16x32_bf16 v[58:61], v[174:177], v[198:201], v[58:61]
	v_mfma_f32_16x16x32_bf16 v[38:41], v[166:169], v[206:209], v[38:41]
	v_mfma_f32_16x16x32_bf16 v[34:37], v[174:177], v[206:209], v[34:37]
	v_mfma_f32_16x16x32_bf16 v[22:25], v[166:169], v[214:217], v[22:25]
	v_mfma_f32_16x16x32_bf16 v[18:21], v[174:177], v[214:217], v[18:21]
	v_mfma_f32_16x16x32_bf16 v[6:9], v[166:169], v[222:225], v[6:9]
	v_mfma_f32_16x16x32_bf16 v[2:5], v[174:177], v[222:225], v[2:5]
	v_mfma_f32_16x16x32_bf16 v[62:65], v[170:173], v[202:205], v[62:65]
	v_mfma_f32_16x16x32_bf16 v[58:61], v[178:181], v[202:205], v[58:61]
	v_mfma_f32_16x16x32_bf16 v[38:41], v[170:173], v[210:213], v[38:41]
	v_mfma_f32_16x16x32_bf16 v[34:37], v[178:181], v[210:213], v[34:37]
	v_mfma_f32_16x16x32_bf16 v[22:25], v[170:173], v[218:221], v[22:25]
	v_mfma_f32_16x16x32_bf16 v[18:21], v[178:181], v[218:221], v[18:21]
	v_mfma_f32_16x16x32_bf16 v[6:9], v[170:173], v[230:233], v[6:9]
	v_mfma_f32_16x16x32_bf16 v[2:5], v[178:181], v[230:233], v[2:5]
	s_setprio 0
	s_setprio 1
	v_mfma_f32_16x16x32_bf16 v[50:53], v[182:185], v[198:201], v[50:53]
	v_mfma_f32_16x16x32_bf16 v[42:45], v[190:193], v[198:201], v[42:45]
	v_mfma_f32_16x16x32_bf16 v[54:57], v[182:185], v[206:209], v[54:57]
	v_mfma_f32_16x16x32_bf16 v[46:49], v[190:193], v[206:209], v[46:49]
	v_mfma_f32_16x16x32_bf16 v[30:33], v[182:185], v[214:217], v[30:33]
	v_mfma_f32_16x16x32_bf16 v[26:29], v[190:193], v[214:217], v[26:29]
	v_mfma_f32_16x16x32_bf16 v[14:17], v[182:185], v[222:225], v[14:17]
	v_mfma_f32_16x16x32_bf16 v[10:13], v[190:193], v[222:225], v[10:13]
	v_mfma_f32_16x16x32_bf16 v[50:53], v[186:189], v[202:205], v[50:53]
	v_mfma_f32_16x16x32_bf16 v[42:45], v[194:197], v[202:205], v[42:45]
	v_mfma_f32_16x16x32_bf16 v[54:57], v[186:189], v[210:213], v[54:57]
	v_mfma_f32_16x16x32_bf16 v[46:49], v[194:197], v[210:213], v[46:49]
	v_mfma_f32_16x16x32_bf16 v[30:33], v[186:189], v[218:221], v[30:33]
	v_mfma_f32_16x16x32_bf16 v[26:29], v[194:197], v[218:221], v[26:29]
	v_mfma_f32_16x16x32_bf16 v[14:17], v[186:189], v[230:233], v[14:17]
	v_mfma_f32_16x16x32_bf16 v[10:13], v[194:197], v[230:233], v[10:13]
	s_setprio 0
	s_barrier
	s_add_i32 s63, s63, 2
	s_add_u32 s40, s40, 0x100
	s_addc_u32 s41, s41, 0
	s_cmp_gt_u32 s63, 13
	s_andn2_b64 vcc, exec, s[6:7]
	s_cbranch_vccnz .Lg5_nonext
	s_waitcnt vmcnt(8)
	v_readfirstlane_b32 s34, v250
	v_lshl_add_u32 v164, v229, 11, v152
	v_lshl_add_u32 v163, v251, 11, v153
	v_lshl_add_u32 v162, v252, 11, v152
	v_lshl_add_u32 v161, v253, 11, v153
	s_mul_i32 s34, s34, 28
	s_add_i32 s30, s34, s30
	s_ashr_i32 s31, s30, 31
	s_lshl_b64 s[34:35], s[30:31], 19
	v_readlane_b32 s42, v254, 29
	v_readlane_b32 s43, v254, 30
	s_add_u32 s34, s42, s34
	s_addc_u32 s35, s43, s35
	s_mov_b32 s29, s35
	s_mov_b32 s31, s34
.Lg5_nonext:
	s_lshl_b32 s42, s38, 8
	s_add_i32 s42, s42, s54
	v_or_b32_e32 v248, s42, v145
	v_ashrrev_i32_e32 v249, 31, v248
	v_lshl_add_u64 v[248:249], v[248:249], 2, s[18:19]
	global_load_dword v240, v[248:249], off offset:704
	global_load_dword v241, v[248:249], off offset:640
	global_load_dword v242, v[248:249], off offset:576
	global_load_dword v243, v[248:249], off offset:512
	global_load_dword v244, v[248:249], off offset:192
	global_load_dword v245, v[248:249], off offset:128
	global_load_dword v246, v[248:249], off offset:64
	global_load_dword v247, v[248:249], off

; __device__ __forceinline__ unsigned cvt_pk_bf16(float lo, float hi) { const f32x2c_t v = {lo, hi}; return __builtin_bit_cast(unsigned, __builtin_convertvector(v, bf16x2c_t)); }
; __device__ __forceinline__ float silu_f(float a) { return a * __builtin_amdgcn_rcpf(1.0f + __builtin_amdgcn_exp2f(a * -1.4426950408889634f)); }
;     __device__ __forceinline__ void operator()(const f32x4 (&acc)[2][2][4][2], const Unit& u, int wr, int wc, int fr, int fq) const {
;         const int row0 = u.pm * BM + wr * 64 + fr; const int pnl = MOE ? (u.pn % 28) : u.pn;
;         const int lane = fr + 16 * fq, qs4 = QSRC_ST(lane); const int rowS = u.pm * BM + wr * 64 + (lane >> 2), colS = pnl * HALF + wc * 32 + 8 * (lane & 3);
;         float rs8[2][4];
;         if constexpr (MOE) {
; #pragma unroll
;             for (int ai = 0; ai < 2; ++ai)
; #pragma unroll
;                 for (int m = 0; m < 4; ++m) rs8[ai][m] = SS[row0 + ai * HALF + m * 16];
;             asm volatile("" : "+v"(rs8[0][0]), "+v"(rs8[0][1]), "+v"(rs8[0][2]), "+v"(rs8[0][3]), "+v"(rs8[1][0]), "+v"(rs8[1][1]), "+v"(rs8[1][2]), "+v"(rs8[1][3]));
;         } else rstd8(SS, u.pm * BM + wr * 64, lane, rs8);
; #pragma unroll
;         for (int ai = 0; ai < 2; ++ai) {
; #pragma unroll
;             for (int m = 0; m < 4; ++m) { const int row = row0 + ai * HALF + m * 16; const float rs = rs8[ai][m];
;                 const f32x4 a0 = acc[ai][0][m][0] * rs, a1 = acc[ai][0][m][1] * rs, b0 = acc[ai][1][m][0] * rs, b1 = acc[ai][1][m][1] * rs;
;                 f32x4 g0, g1;
; #pragma unroll
;                 for (int j = 0; j < 4; ++j) { g0[j] = silu_f(a0[j]) * b0[j]; g1[j] = silu_f(a1[j]) * b1[j]; }
;                 u32x4 w; w.x = cvt_pk_bf16(g0[0], g0[1]); w.y = cvt_pk_bf16(g0[2], g0[3]); w.z = cvt_pk_bf16(g1[0], g1[1]); w.w = cvt_pk_bf16(g1[2], g1[3]);
;                 w = lane_perm(w, qs4); u32x4* dst = (u32x4*)(O + (size_t)(rowS + ai * HALF + m * 16) * ldo + colS); (void)row;
.LBB0_1731:
	s_lshl_b32 s6, s38, 8
	s_add_i32 s6, s6, s54
	s_mul_hi_i32 s7, s36, 0x92492493
	v_readlane_b32 s40, v254, 36
	s_add_i32 s7, s7, s36
	v_readlane_b32 s41, v254, 37
	v_or_b32_e32 v147, s6, v155
	s_lshr_b32 s6, s7, 31
	s_lshr_b32 s7, s7, 4
	v_mov_b64_e32 v[140:141], s[40:41]
	s_add_i32 s29, s7, s6
	v_mad_i64_i32 v[170:171], s[6:7], v147, s60, v[140:141]
	s_mul_i32 s29, s29, 28
	s_sub_i32 s6, s36, s29
	v_lshl_or_b32 v142, s6, 7, v157
	v_ashrrev_i32_e32 v143, 31, v142
	v_lshlrev_b64 v[142:143], 1, v[142:143]
	v_lshl_add_u64 v[170:171], v[170:171], 0, v[142:143]
	v_mul_f32_e32 v248, 0xbfb8aa3b, v247
	v_mul_f32_e32 v250, v247, v247
	v_rcp_f32_e32 v250, v250
	v_pk_mul_f32 v[118:119], v[118:119], v[126:127]
	v_pk_mul_f32 v[120:121], v[120:121], v[128:129]
	v_pk_mul_f32 v[114:115], v[114:115], v[122:123]
	v_pk_mul_f32 v[116:117], v[116:117], v[124:125]
	v_pk_mul_f32 v[126:127], v[126:127], v[248:249] op_sel_hi:[1,0]
	v_pk_mul_f32 v[128:129], v[128:129], v[248:249] op_sel_hi:[1,0]
	v_pk_mul_f32 v[122:123], v[122:123], v[248:249] op_sel_hi:[1,0]
	v_pk_mul_f32 v[124:125], v[124:125], v[248:249] op_sel_hi:[1,0]
	v_exp_f32_e32 v126, v126
	v_exp_f32_e32 v127, v127
	v_exp_f32_e32 v128, v128
	v_exp_f32_e32 v129, v129
	v_exp_f32_e32 v122, v122
	v_exp_f32_e32 v123, v123
	v_exp_f32_e32 v124, v124
	v_exp_f32_e32 v125, v125
	v_pk_fma_f32 v[126:127], v[126:127], v[250:251], v[250:251] op_sel_hi:[1,0,0]
	v_pk_fma_f32 v[128:129], v[128:129], v[250:251], v[250:251] op_sel_hi:[1,0,0]
	v_pk_fma_f32 v[122:123], v[122:123], v[250:251], v[250:251] op_sel_hi:[1,0,0]
	v_pk_fma_f32 v[124:125], v[124:125], v[250:251], v[250:251] op_sel_hi:[1,0,0]
	v_rcp_f32_e32 v126, v126
	v_rcp_f32_e32 v127, v127
	v_rcp_f32_e32 v128, v128
	v_rcp_f32_e32 v129, v129
	v_rcp_f32_e32 v122, v122
	v_rcp_f32_e32 v123, v123
	v_rcp_f32_e32 v124, v124
	v_rcp_f32_e32 v125, v125
	v_pk_mul_f32 v[118:119], v[118:119], v[126:127]
	v_pk_mul_f32 v[120:121], v[120:121], v[128:129]
	v_pk_mul_f32 v[114:115], v[114:115], v[122:123]
	v_pk_mul_f32 v[116:117], v[116:117], v[124:125]
	v_cvt_pk_bf16_f32 v126, v118, v119
	v_cvt_pk_bf16_f32 v127, v120, v121
	v_cvt_pk_bf16_f32 v128, v114, v115
	v_cvt_pk_bf16_f32 v129, v116, v117
	ds_bpermute_b32 v122, v156, v126
	ds_bpermute_b32 v123, v156, v127
	ds_bpermute_b32 v124, v156, v128
	ds_bpermute_b32 v125, v156, v129
	v_mov_b32_e32 v140, v170
	v_mov_b32_e32 v141, v171
	v_mul_f32_e32 v248, 0xbfb8aa3b, v246
	v_mul_f32_e32 v250, v246, v246
	v_rcp_f32_e32 v250, v250
	v_pk_mul_f32 v[102:103], v[102:103], v[110:111]
	v_pk_mul_f32 v[104:105], v[104:105], v[112:113]
	v_pk_mul_f32 v[98:99], v[98:99], v[106:107]
	v_pk_mul_f32 v[100:101], v[100:101], v[108:109]
	v_pk_mul_f32 v[110:111], v[110:111], v[248:249] op_sel_hi:[1,0]
	v_pk_mul_f32 v[112:113], v[112:113], v[248:249] op_sel_hi:[1,0]
	v_pk_mul_f32 v[106:107], v[106:107], v[248:249] op_sel_hi:[1,0]
	v_pk_mul_f32 v[108:109], v[108:109], v[248:249] op_sel_hi:[1,0]
	v_exp_f32_e32 v110, v110
	v_exp_f32_e32 v111, v111
	v_exp_f32_e32 v112, v112
	v_exp_f32_e32 v113, v113
	v_exp_f32_e32 v106, v106
	v_exp_f32_e32 v107, v107
	v_exp_f32_e32 v108, v108
	v_exp_f32_e32 v109, v109
	v_pk_fma_f32 v[110:111], v[110:111], v[250:251], v[250:251] op_sel_hi:[1,0,0]
	v_pk_fma_f32 v[112:113], v[112:113], v[250:251], v[250:251] op_sel_hi:[1,0,0]
	v_pk_fma_f32 v[106:107], v[106:107], v[250:251], v[250:251] op_sel_hi:[1,0,0]
	v_pk_fma_f32 v[108:109], v[108:109], v[250:251], v[250:251] op_sel_hi:[1,0,0]
	v_rcp_f32_e32 v110, v110
	v_rcp_f32_e32 v111, v111
	v_rcp_f32_e32 v112, v112
	v_rcp_f32_e32 v113, v113
	v_rcp_f32_e32 v106, v106
	v_rcp_f32_e32 v107, v107
	v_rcp_f32_e32 v108, v108
	v_rcp_f32_e32 v109, v109
	v_pk_mul_f32 v[102:103], v[102:103], v[110:111]
	v_pk_mul_f32 v[104:105], v[104:105], v[112:113]
	v_pk_mul_f32 v[98:99], v[98:99], v[106:107]
	v_pk_mul_f32 v[100:101], v[100:101], v[108:109]
	s_waitcnt lgkmcnt(0)
	global_store_dwordx4 v[140:141], v[122:125], off nt
	v_cvt_pk_bf16_f32 v110, v102, v103
	v_cvt_pk_bf16_f32 v111, v104, v105
	v_cvt_pk_bf16_f32 v112, v98, v99
	v_cvt_pk_bf16_f32 v113, v100, v101
	ds_bpermute_b32 v106, v156, v110
	ds_bpermute_b32 v107, v156, v111
	ds_bpermute_b32 v108, v156, v112
	ds_bpermute_b32 v109, v156, v113
	v_add_co_u32_e32 v142, vcc, 0x1c000, v170
	v_addc_co_u32_e32 v143, vcc, 0, v171, vcc
	v_mul_f32_e32 v248, 0xbfb8aa3b, v245
	v_mul_f32_e32 v250, v245, v245
	v_rcp_f32_e32 v250, v250
	v_pk_mul_f32 v[86:87], v[86:87], v[94:95]
	v_pk_mul_f32 v[88:89], v[88:89], v[96:97]
	v_pk_mul_f32 v[82:83], v[82:83], v[90:91]
	v_pk_mul_f32 v[84:85], v[84:85], v[92:93]
	v_pk_mul_f32 v[94:95], v[94:95], v[248:249] op_sel_hi:[1,0]
	v_pk_mul_f32 v[96:97], v[96:97], v[248:249] op_sel_hi:[1,0]
	v_pk_mul_f32 v[90:91], v[90:91], v[248:249] op_sel_hi:[1,0]
	v_pk_mul_f32 v[92:93], v[92:93], v[248:249] op_sel_hi:[1,0]
	v_exp_f32_e32 v94, v94
	v_exp_f32_e32 v95, v95
	v_exp_f32_e32 v96, v96
	v_exp_f32_e32 v97, v97
	v_exp_f32_e32 v90, v90
	v_exp_f32_e32 v91, v91
	v_exp_f32_e32 v92, v92
	v_exp_f32_e32 v93, v93
	v_pk_fma_f32 v[94:95], v[94:95], v[250:251], v[250:251] op_sel_hi:[1,0,0]
	v_pk_fma_f32 v[96:97], v[96:97], v[250:251], v[250:251] op_sel_hi:[1,0,0]
	v_pk_fma_f32 v[90:91], v[90:91], v[250:251], v[250:251] op_sel_hi:[1,0,0]
	v_pk_fma_f32 v[92:93], v[92:93], v[250:251], v[250:251] op_sel_hi:[1,0,0]
	v_rcp_f32_e32 v94, v94
	v_rcp_f32_e32 v95, v95
	v_rcp_f32_e32 v96, v96
	v_rcp_f32_e32 v97, v97
	v_rcp_f32_e32 v90, v90
	v_rcp_f32_e32 v91, v91
	v_rcp_f32_e32 v92, v92
	v_rcp_f32_e32 v93, v93
	v_pk_mul_f32 v[86:87], v[86:87], v[94:95]
	v_pk_mul_f32 v[88:89], v[88:89], v[96:97]
	v_pk_mul_f32 v[82:83], v[82:83], v[90:91]
	v_pk_mul_f32 v[84:85], v[84:85], v[92:93]
	s_waitcnt lgkmcnt(0)
; __device__ __forceinline__ unsigned cvt_pk_bf16(float lo, float hi) { const f32x2c_t v = {lo, hi}; return __builtin_bit_cast(unsigned, __builtin_convertvector(v, bf16x2c_t)); }
; __device__ __forceinline__ float silu_f(float a) { return a * __builtin_amdgcn_rcpf(1.0f + __builtin_amdgcn_exp2f(a * -1.4426950408889634f)); }
;     __device__ __forceinline__ void operator()(const f32x4 (&acc)[2][2][4][2], const Unit& u, int wr, int wc, int fr, int fq) const {
;     ...
;         for (int ai = 0; ai < 2; ++ai) {
; #pragma unroll
;             for (int m = 0; m < 4; ++m) { const int row = row0 + ai * HALF + m * 16; const float rs = rs8[ai][m];
;                 const f32x4 a0 = acc[ai][0][m][0] * rs, a1 = acc[ai][0][m][1] * rs, b0 = acc[ai][1][m][0] * rs, b1 = acc[ai][1][m][1] * rs;
;                 f32x4 g0, g1;
; #pragma unroll
;                 for (int j = 0; j < 4; ++j) { g0[j] = silu_f(a0[j]) * b0[j]; g1[j] = silu_f(a1[j]) * b1[j]; }
;                 u32x4 w; w.x = cvt_pk_bf16(g0[0], g0[1]); w.y = cvt_pk_bf16(g0[2], g0[3]); w.z = cvt_pk_bf16(g1[0], g1[1]); w.w = cvt_pk_bf16(g1[2], g1[3]);
;                 w = lane_perm(w, qs4); u32x4* dst = (u32x4*)(O + (size_t)(rowS + ai * HALF + m * 16) * ldo + colS); (void)row;
	global_store_dwordx4 v[142:143], v[106:109], off nt
	v_cvt_pk_bf16_f32 v94, v86, v87
	v_cvt_pk_bf16_f32 v95, v88, v89
	v_cvt_pk_bf16_f32 v96, v82, v83
	v_cvt_pk_bf16_f32 v97, v84, v85
	ds_bpermute_b32 v90, v156, v94
	ds_bpermute_b32 v91, v156, v95
	ds_bpermute_b32 v92, v156, v96
	ds_bpermute_b32 v93, v156, v97
	v_add_co_u32_e32 v140, vcc, 0x38000, v170
	v_addc_co_u32_e32 v141, vcc, 0, v171, vcc
	v_mul_f32_e32 v248, 0xbfb8aa3b, v244
	v_mul_f32_e32 v250, v244, v244
	v_rcp_f32_e32 v250, v250
	v_pk_mul_f32 v[70:71], v[70:71], v[78:79]
	v_pk_mul_f32 v[72:73], v[72:73], v[80:81]
	v_pk_mul_f32 v[66:67], v[66:67], v[74:75]
	v_pk_mul_f32 v[68:69], v[68:69], v[76:77]
	v_pk_mul_f32 v[78:79], v[78:79], v[248:249] op_sel_hi:[1,0]
	v_pk_mul_f32 v[80:81], v[80:81], v[248:249] op_sel_hi:[1,0]
	v_pk_mul_f32 v[74:75], v[74:75], v[248:249] op_sel_hi:[1,0]
	v_pk_mul_f32 v[76:77], v[76:77], v[248:249] op_sel_hi:[1,0]
	v_exp_f32_e32 v78, v78
	v_exp_f32_e32 v79, v79
	v_exp_f32_e32 v80, v80
	v_exp_f32_e32 v81, v81
	v_exp_f32_e32 v74, v74
	v_exp_f32_e32 v75, v75
	v_exp_f32_e32 v76, v76
	v_exp_f32_e32 v77, v77
	v_pk_fma_f32 v[78:79], v[78:79], v[250:251], v[250:251] op_sel_hi:[1,0,0]
	v_pk_fma_f32 v[80:81], v[80:81], v[250:251], v[250:251] op_sel_hi:[1,0,0]
	v_pk_fma_f32 v[74:75], v[74:75], v[250:251], v[250:251] op_sel_hi:[1,0,0]
	v_pk_fma_f32 v[76:77], v[76:77], v[250:251], v[250:251] op_sel_hi:[1,0,0]
	v_rcp_f32_e32 v78, v78
	v_rcp_f32_e32 v79, v79
	v_rcp_f32_e32 v80, v80
	v_rcp_f32_e32 v81, v81
	v_rcp_f32_e32 v74, v74
	v_rcp_f32_e32 v75, v75
	v_rcp_f32_e32 v76, v76
	v_rcp_f32_e32 v77, v77
	v_pk_mul_f32 v[70:71], v[70:71], v[78:79]
	v_pk_mul_f32 v[72:73], v[72:73], v[80:81]
	v_pk_mul_f32 v[66:67], v[66:67], v[74:75]
	v_pk_mul_f32 v[68:69], v[68:69], v[76:77]
	s_waitcnt lgkmcnt(0)
	global_store_dwordx4 v[140:141], v[90:93], off nt
	v_cvt_pk_bf16_f32 v78, v70, v71
	v_cvt_pk_bf16_f32 v79, v72, v73
	v_cvt_pk_bf16_f32 v80, v66, v67
	v_cvt_pk_bf16_f32 v81, v68, v69
	ds_bpermute_b32 v74, v156, v78
	ds_bpermute_b32 v75, v156, v79
	ds_bpermute_b32 v76, v156, v80
	ds_bpermute_b32 v77, v156, v81
	v_add_co_u32_e32 v142, vcc, 0x54000, v170
	v_addc_co_u32_e32 v143, vcc, 0, v171, vcc
	v_mul_f32_e32 v248, 0xbfb8aa3b, v243
	v_mul_f32_e32 v250, v243, v243
	v_rcp_f32_e32 v250, v250
	v_pk_mul_f32 v[50:51], v[50:51], v[62:63]
	v_pk_mul_f32 v[52:53], v[52:53], v[64:65]
	v_pk_mul_f32 v[42:43], v[42:43], v[58:59]
	v_pk_mul_f32 v[44:45], v[44:45], v[60:61]
	v_pk_mul_f32 v[62:63], v[62:63], v[248:249] op_sel_hi:[1,0]
	v_pk_mul_f32 v[64:65], v[64:65], v[248:249] op_sel_hi:[1,0]
	v_pk_mul_f32 v[58:59], v[58:59], v[248:249] op_sel_hi:[1,0]
	v_pk_mul_f32 v[60:61], v[60:61], v[248:249] op_sel_hi:[1,0]
	v_exp_f32_e32 v62, v62
	v_exp_f32_e32 v63, v63
	v_exp_f32_e32 v64, v64
	v_exp_f32_e32 v65, v65
	v_exp_f32_e32 v58, v58
	v_exp_f32_e32 v59, v59
	v_exp_f32_e32 v60, v60
	v_exp_f32_e32 v61, v61
	v_pk_fma_f32 v[62:63], v[62:63], v[250:251], v[250:251] op_sel_hi:[1,0,0]
	v_pk_fma_f32 v[64:65], v[64:65], v[250:251], v[250:251] op_sel_hi:[1,0,0]
	v_pk_fma_f32 v[58:59], v[58:59], v[250:251], v[250:251] op_sel_hi:[1,0,0]
	v_pk_fma_f32 v[60:61], v[60:61], v[250:251], v[250:251] op_sel_hi:[1,0,0]
	v_rcp_f32_e32 v62, v62
	v_rcp_f32_e32 v63, v63
	v_rcp_f32_e32 v64, v64
	v_rcp_f32_e32 v65, v65
	v_rcp_f32_e32 v58, v58
	v_rcp_f32_e32 v59, v59
	v_rcp_f32_e32 v60, v60
	v_rcp_f32_e32 v61, v61
	v_pk_mul_f32 v[50:51], v[50:51], v[62:63]
	v_pk_mul_f32 v[52:53], v[52:53], v[64:65]
	v_pk_mul_f32 v[42:43], v[42:43], v[58:59]
	v_pk_mul_f32 v[44:45], v[44:45], v[60:61]
	s_waitcnt lgkmcnt(0)
	global_store_dwordx4 v[142:143], v[74:77], off nt
	v_cvt_pk_bf16_f32 v62, v50, v51
	v_cvt_pk_bf16_f32 v63, v52, v53
	v_cvt_pk_bf16_f32 v64, v42, v43
	v_cvt_pk_bf16_f32 v65, v44, v45
	ds_bpermute_b32 v58, v156, v62
	ds_bpermute_b32 v59, v156, v63
	ds_bpermute_b32 v60, v156, v64
	ds_bpermute_b32 v61, v156, v65
	v_add_co_u32_e32 v140, vcc, 0xe0000, v170
	v_addc_co_u32_e32 v141, vcc, 0, v171, vcc
	v_mul_f32_e32 v248, 0xbfb8aa3b, v242
	v_mul_f32_e32 v250, v242, v242
	v_rcp_f32_e32 v250, v250
	v_pk_mul_f32 v[54:55], v[54:55], v[38:39]
	v_pk_mul_f32 v[56:57], v[56:57], v[40:41]
	v_pk_mul_f32 v[46:47], v[46:47], v[34:35]
	v_pk_mul_f32 v[48:49], v[48:49], v[36:37]
	v_pk_mul_f32 v[38:39], v[38:39], v[248:249] op_sel_hi:[1,0]
	v_pk_mul_f32 v[40:41], v[40:41], v[248:249] op_sel_hi:[1,0]
	v_pk_mul_f32 v[34:35], v[34:35], v[248:249] op_sel_hi:[1,0]
	v_pk_mul_f32 v[36:37], v[36:37], v[248:249] op_sel_hi:[1,0]
	v_exp_f32_e32 v38, v38
	v_exp_f32_e32 v39, v39
	v_exp_f32_e32 v40, v40
	v_exp_f32_e32 v41, v41
	v_exp_f32_e32 v34, v34
	v_exp_f32_e32 v35, v35
	v_exp_f32_e32 v36, v36
	v_exp_f32_e32 v37, v37
	v_pk_fma_f32 v[38:39], v[38:39], v[250:251], v[250:251] op_sel_hi:[1,0,0]
	v_pk_fma_f32 v[40:41], v[40:41], v[250:251], v[250:251] op_sel_hi:[1,0,0]
	v_pk_fma_f32 v[34:35], v[34:35], v[250:251], v[250:251] op_sel_hi:[1,0,0]
	v_pk_fma_f32 v[36:37], v[36:37], v[250:251], v[250:251] op_sel_hi:[1,0,0]
	v_rcp_f32_e32 v38, v38
	v_rcp_f32_e32 v39, v39
	v_rcp_f32_e32 v40, v40
	v_rcp_f32_e32 v41, v41
	v_rcp_f32_e32 v34, v34
	v_rcp_f32_e32 v35, v35
	v_rcp_f32_e32 v36, v36
	v_rcp_f32_e32 v37, v37
	v_pk_mul_f32 v[54:55], v[54:55], v[38:39]
	v_pk_mul_f32 v[56:57], v[56:57], v[40:41]
	v_pk_mul_f32 v[46:47], v[46:47], v[34:35]
	v_pk_mul_f32 v[48:49], v[48:49], v[36:37]
	s_waitcnt lgkmcnt(0)
	global_store_dwordx4 v[140:141], v[58:61], off nt
	v_cvt_pk_bf16_f32 v38, v54, v55
	v_cvt_pk_bf16_f32 v39, v56, v57
	v_cvt_pk_bf16_f32 v40, v46, v47
	v_cvt_pk_bf16_f32 v41, v48, v49
	ds_bpermute_b32 v34, v156, v38
	ds_bpermute_b32 v35, v156, v39
	ds_bpermute_b32 v36, v156, v40
	ds_bpermute_b32 v37, v156, v41
	v_add_co_u32_e32 v142, vcc, 0xfc000, v170
	v_addc_co_u32_e32 v143, vcc, 0, v171, vcc
	s_and_b64 vcc, exec, s[4:5]
	s_cbranch_vccz .Lg5_defer
; __device__ __forceinline__ unsigned cvt_pk_bf16(float lo, float hi) { const f32x2c_t v = {lo, hi}; return __builtin_bit_cast(unsigned, __builtin_convertvector(v, bf16x2c_t)); }
; __device__ __forceinline__ float silu_f(float a) { return a * __builtin_amdgcn_rcpf(1.0f + __builtin_amdgcn_exp2f(a * -1.4426950408889634f)); }
;     __device__ __forceinline__ void operator()(const f32x4 (&acc)[2][2][4][2], const Unit& u, int wr, int wc, int fr, int fq) const {
;     ...
;         for (int ai = 0; ai < 2; ++ai) {
; #pragma unroll
;             for (int m = 0; m < 4; ++m) { const int row = row0 + ai * HALF + m * 16; const float rs = rs8[ai][m];
;                 const f32x4 a0 = acc[ai][0][m][0] * rs, a1 = acc[ai][0][m][1] * rs, b0 = acc[ai][1][m][0] * rs, b1 = acc[ai][1][m][1] * rs;
;                 f32x4 g0, g1;
; #pragma unroll
;                 for (int j = 0; j < 4; ++j) { g0[j] = silu_f(a0[j]) * b0[j]; g1[j] = silu_f(a1[j]) * b1[j]; }
;                 u32x4 w; w.x = cvt_pk_bf16(g0[0], g0[1]); w.y = cvt_pk_bf16(g0[2], g0[3]); w.z = cvt_pk_bf16(g1[0], g1[1]); w.w = cvt_pk_bf16(g1[2], g1[3]);
;                 w = lane_perm(w, qs4); u32x4* dst = (u32x4*)(O + (size_t)(rowS + ai * HALF + m * 16) * ldo + colS); (void)row;
;                 if constexpr (MOE) __builtin_nontemporal_store(w, dst); else *dst = w; } }
	v_mul_f32_e32 v248, 0xbfb8aa3b, v241
	v_mul_f32_e32 v250, v241, v241
	v_rcp_f32_e32 v250, v250
	v_pk_mul_f32 v[30:31], v[30:31], v[22:23]
	v_pk_mul_f32 v[32:33], v[32:33], v[24:25]
	v_pk_mul_f32 v[26:27], v[26:27], v[18:19]
	v_pk_mul_f32 v[28:29], v[28:29], v[20:21]
	v_pk_mul_f32 v[22:23], v[22:23], v[248:249] op_sel_hi:[1,0]
	v_pk_mul_f32 v[24:25], v[24:25], v[248:249] op_sel_hi:[1,0]
	v_pk_mul_f32 v[18:19], v[18:19], v[248:249] op_sel_hi:[1,0]
	v_pk_mul_f32 v[20:21], v[20:21], v[248:249] op_sel_hi:[1,0]
	v_exp_f32_e32 v22, v22
	v_exp_f32_e32 v23, v23
	v_exp_f32_e32 v24, v24
	v_exp_f32_e32 v25, v25
	v_exp_f32_e32 v18, v18
	v_exp_f32_e32 v19, v19
	v_exp_f32_e32 v20, v20
	v_exp_f32_e32 v21, v21
	v_pk_fma_f32 v[22:23], v[22:23], v[250:251], v[250:251] op_sel_hi:[1,0,0]
	v_pk_fma_f32 v[24:25], v[24:25], v[250:251], v[250:251] op_sel_hi:[1,0,0]
	v_pk_fma_f32 v[18:19], v[18:19], v[250:251], v[250:251] op_sel_hi:[1,0,0]
	v_pk_fma_f32 v[20:21], v[20:21], v[250:251], v[250:251] op_sel_hi:[1,0,0]
	v_rcp_f32_e32 v22, v22
	v_rcp_f32_e32 v23, v23
	v_rcp_f32_e32 v24, v24
	v_rcp_f32_e32 v25, v25
	v_rcp_f32_e32 v18, v18
	v_rcp_f32_e32 v19, v19
	v_rcp_f32_e32 v20, v20
	v_rcp_f32_e32 v21, v21
	v_pk_mul_f32 v[30:31], v[30:31], v[22:23]
	v_pk_mul_f32 v[32:33], v[32:33], v[24:25]
	v_pk_mul_f32 v[26:27], v[26:27], v[18:19]
	v_pk_mul_f32 v[28:29], v[28:29], v[20:21]
	s_waitcnt lgkmcnt(0)
	global_store_dwordx4 v[142:143], v[34:37], off nt
	v_cvt_pk_bf16_f32 v22, v30, v31
	v_cvt_pk_bf16_f32 v23, v32, v33
	v_cvt_pk_bf16_f32 v24, v26, v27
	v_cvt_pk_bf16_f32 v25, v28, v29
	ds_bpermute_b32 v18, v156, v22
	ds_bpermute_b32 v19, v156, v23
	ds_bpermute_b32 v20, v156, v24
	ds_bpermute_b32 v21, v156, v25
	v_add_co_u32_e32 v140, vcc, 0x118000, v170
	v_addc_co_u32_e32 v141, vcc, 0, v171, vcc
	v_mul_f32_e32 v248, 0xbfb8aa3b, v240
	v_mul_f32_e32 v250, v240, v240
	v_rcp_f32_e32 v250, v250
	v_pk_mul_f32 v[14:15], v[14:15], v[6:7]
	v_pk_mul_f32 v[16:17], v[16:17], v[8:9]
	v_pk_mul_f32 v[10:11], v[10:11], v[2:3]
	v_pk_mul_f32 v[12:13], v[12:13], v[4:5]
	v_pk_mul_f32 v[6:7], v[6:7], v[248:249] op_sel_hi:[1,0]
	v_pk_mul_f32 v[8:9], v[8:9], v[248:249] op_sel_hi:[1,0]
	v_pk_mul_f32 v[2:3], v[2:3], v[248:249] op_sel_hi:[1,0]
	v_pk_mul_f32 v[4:5], v[4:5], v[248:249] op_sel_hi:[1,0]
	v_exp_f32_e32 v6, v6
	v_exp_f32_e32 v7, v7
	v_exp_f32_e32 v8, v8
	v_exp_f32_e32 v9, v9
	v_exp_f32_e32 v2, v2
	v_exp_f32_e32 v3, v3
	v_exp_f32_e32 v4, v4
	v_exp_f32_e32 v5, v5
	v_pk_fma_f32 v[6:7], v[6:7], v[250:251], v[250:251] op_sel_hi:[1,0,0]
	v_pk_fma_f32 v[8:9], v[8:9], v[250:251], v[250:251] op_sel_hi:[1,0,0]
	v_pk_fma_f32 v[2:3], v[2:3], v[250:251], v[250:251] op_sel_hi:[1,0,0]
	v_pk_fma_f32 v[4:5], v[4:5], v[250:251], v[250:251] op_sel_hi:[1,0,0]
	v_rcp_f32_e32 v6, v6
	v_rcp_f32_e32 v7, v7
	v_rcp_f32_e32 v8, v8
	v_rcp_f32_e32 v9, v9
	v_rcp_f32_e32 v2, v2
	v_rcp_f32_e32 v3, v3
	v_rcp_f32_e32 v4, v4
	v_rcp_f32_e32 v5, v5
	v_pk_mul_f32 v[14:15], v[14:15], v[6:7]
	v_pk_mul_f32 v[16:17], v[16:17], v[8:9]
	v_pk_mul_f32 v[10:11], v[10:11], v[2:3]
	v_pk_mul_f32 v[12:13], v[12:13], v[4:5]
	s_waitcnt lgkmcnt(0)
	global_store_dwordx4 v[140:141], v[18:21], off nt
	v_cvt_pk_bf16_f32 v6, v14, v15
	v_cvt_pk_bf16_f32 v7, v16, v17
	v_cvt_pk_bf16_f32 v8, v10, v11
	v_cvt_pk_bf16_f32 v9, v12, v13
	ds_bpermute_b32 v2, v156, v6
	ds_bpermute_b32 v3, v156, v7
	ds_bpermute_b32 v4, v156, v8
	ds_bpermute_b32 v5, v156, v9
	v_add_co_u32_e32 v142, vcc, 0x134000, v170
	v_addc_co_u32_e32 v143, vcc, 0, v171, vcc
	s_waitcnt lgkmcnt(0)
	global_store_dwordx4 v[142:143], v[2:5], off nt
	s_branch .Lg5_epi_end
.Lg5_defer:
	v_mul_f32_e32 v248, 0xbfb8aa3b, v241
	v_mul_f32_e32 v250, v241, v241
	v_pk_mul_f32 v[30:31], v[30:31], v[22:23]
	v_pk_mul_f32 v[32:33], v[32:33], v[24:25]
	v_pk_mul_f32 v[26:27], v[26:27], v[18:19]
	v_pk_mul_f32 v[28:29], v[28:29], v[20:21]
	v_pk_mul_f32 v[22:23], v[22:23], v[248:249] op_sel_hi:[1,0]
	v_pk_mul_f32 v[24:25], v[24:25], v[248:249] op_sel_hi:[1,0]
	v_pk_mul_f32 v[18:19], v[18:19], v[248:249] op_sel_hi:[1,0]
	v_pk_mul_f32 v[20:21], v[20:21], v[248:249] op_sel_hi:[1,0]
	v_pk_mul_f32 v[30:31], v[30:31], v[250:251] op_sel_hi:[1,0]
	v_pk_mul_f32 v[32:33], v[32:33], v[250:251] op_sel_hi:[1,0]
	v_pk_mul_f32 v[26:27], v[26:27], v[250:251] op_sel_hi:[1,0]
	v_pk_mul_f32 v[28:29], v[28:29], v[250:251] op_sel_hi:[1,0]
	v_mul_f32_e32 v248, 0xbfb8aa3b, v240
	v_mul_f32_e32 v250, v240, v240
	v_pk_mul_f32 v[14:15], v[14:15], v[6:7]
	v_pk_mul_f32 v[16:17], v[16:17], v[8:9]
	v_pk_mul_f32 v[10:11], v[10:11], v[2:3]
	v_pk_mul_f32 v[12:13], v[12:13], v[4:5]
	v_pk_mul_f32 v[6:7], v[6:7], v[248:249] op_sel_hi:[1,0]
	v_pk_mul_f32 v[8:9], v[8:9], v[248:249] op_sel_hi:[1,0]
	v_pk_mul_f32 v[2:3], v[2:3], v[248:249] op_sel_hi:[1,0]
	v_pk_mul_f32 v[4:5], v[4:5], v[248:249] op_sel_hi:[1,0]
	v_pk_mul_f32 v[14:15], v[14:15], v[250:251] op_sel_hi:[1,0]
	v_pk_mul_f32 v[16:17], v[16:17], v[250:251] op_sel_hi:[1,0]
	v_pk_mul_f32 v[10:11], v[10:11], v[250:251] op_sel_hi:[1,0]
	v_pk_mul_f32 v[12:13], v[12:13], v[250:251] op_sel_hi:[1,0]
	s_waitcnt lgkmcnt(0)
	global_store_dwordx4 v[142:143], v[34:37], off nt
	v_add_co_u32_e32 v240, vcc, 0x118000, v170
	v_addc_co_u32_e32 v241, vcc, 0, v171, vcc
	v_add_co_u32_e32 v242, vcc, 0x134000, v170
	v_addc_co_u32_e32 v243, vcc, 0, v171, vcc
	s_mov_b32 s98, 1
.Lg5_epi_end:
	s_and_b64 vcc, exec, s[4:5]
	s_mov_b64 s[4:5], -1
	s_cbranch_vccnz .LBB0_1718
	s_andn2_b64 vcc, exec, s[10:11]
	s_cbranch_vccnz .LBB0_1717
	s_barrier
	s_branch .LBB0_1717

; __global__ void __launch_bounds__(NTHR, 2) hybrid_fwd(Args args) {
	.amdhsa_kernel _Z10hybrid_fwd4Args
		.amdhsa_group_segment_fixed_size 0
		.amdhsa_private_segment_fixed_size 0
		.amdhsa_kernarg_size 432
		.amdhsa_user_sgpr_count 2
		.amdhsa_user_sgpr_dispatch_ptr 0
		.amdhsa_user_sgpr_queue_ptr 0
		.amdhsa_user_sgpr_kernarg_segment_ptr 1
		.amdhsa_user_sgpr_dispatch_id 0
		.amdhsa_user_sgpr_kernarg_preload_length 0
		.amdhsa_user_sgpr_kernarg_preload_offset 0
		.amdhsa_user_sgpr_private_segment_size 0
		.amdhsa_uses_dynamic_stack 0
		.amdhsa_enable_private_segment 0
		.amdhsa_system_sgpr_workgroup_id_x 1
		.amdhsa_system_sgpr_workgroup_id_y 0
		.amdhsa_system_sgpr_workgroup_id_z 0
		.amdhsa_system_sgpr_workgroup_info 0
		.amdhsa_system_vgpr_workitem_id 0
		.amdhsa_next_free_vgpr 256
		.amdhsa_next_free_sgpr 99
		.amdhsa_accum_offset 256
		.amdhsa_reserve_vcc 1
		.amdhsa_float_round_mode_32 0
		.amdhsa_float_round_mode_16_64 0
		.amdhsa_float_denorm_mode_32 3
		.amdhsa_float_denorm_mode_16_64 3
		.amdhsa_dx10_clamp 1
		.amdhsa_ieee_mode 1
		.amdhsa_fp16_overflow 0
		.amdhsa_tg_split 0
		.amdhsa_exception_fp_ieee_invalid_op 0
		.amdhsa_exception_fp_denorm_src 0
		.amdhsa_exception_fp_ieee_div_zero 0
		.amdhsa_exception_fp_ieee_overflow 0
		.amdhsa_exception_fp_ieee_underflow 0
		.amdhsa_exception_fp_ieee_inexact 0
		.amdhsa_exception_int_div_zero 0
	.end_amdhsa_kernel

; __global__ void __launch_bounds__(NTHR, 2) hybrid_fwd(Args args) {
amdhsa.kernels:
  - .agpr_count:     0
    .args:
      - .offset:         0
        .size:           176
        .value_kind:     by_value
      - .offset:         176
        .size:           4
        .value_kind:     hidden_block_count_x
      - .offset:         180
        .size:           4
        .value_kind:     hidden_block_count_y
      - .offset:         184
        .size:           4
        .value_kind:     hidden_block_count_z
      - .offset:         188
        .size:           2
        .value_kind:     hidden_group_size_x
      - .offset:         190
        .size:           2
        .value_kind:     hidden_group_size_y
      - .offset:         192
        .size:           2
        .value_kind:     hidden_group_size_z
      - .offset:         194
        .size:           2
        .value_kind:     hidden_remainder_x
      - .offset:         196
        .size:           2
        .value_kind:     hidden_remainder_y
      - .offset:         198
        .size:           2
        .value_kind:     hidden_remainder_z
      - .offset:         216
        .size:           8
        .value_kind:     hidden_global_offset_x
      - .offset:         224
        .size:           8
        .value_kind:     hidden_global_offset_y
      - .offset:         232
        .size:           8
        .value_kind:     hidden_global_offset_z
      - .offset:         240
        .size:           2
        .value_kind:     hidden_grid_dims
      - .offset:         296
        .size:           4
        .value_kind:     hidden_dynamic_lds_size
    .group_segment_fixed_size: 0
    .kernarg_segment_align: 8
    .kernarg_segment_size: 432
    .language:       OpenCL C
    .language_version:
      - 2
      - 0
    .max_flat_workgroup_size: 512
    .name:           _Z10hybrid_fwd4Args
    .private_segment_fixed_size: 0
    .sgpr_count:     105
    .sgpr_spill_count: 95
    .symbol:         _Z10hybrid_fwd4Args.kd
    .uniform_work_group_size: 1
    .uses_dynamic_stack: false
    .vgpr_count:     256
    .vgpr_spill_count: 0
    .wavefront_size: 64
